# diff attention finalize: the 15 gain-vector loads (each was followed by vmcnt(0) = store+load round trip) hoisted/prefetched into free registers
# speedup vs baseline: 1.0007x; 1.0007x over previous
.LBB0_1026:
	v_readlane_b32 s6, v253, 10
	v_readlane_b32 s7, v253, 11
	s_andn2_b64 vcc, exec, s[6:7]
	s_waitcnt lgkmcnt(0)
	s_barrier
	s_cbranch_vccnz .LBB0_1000
	ds_read2st64_b32 v[74:75], v243 offset1:1
	ds_read2st64_b32 v[76:77], v243 offset0:2 offset1:3
	ds_read2st64_b32 v[78:79], v243 offset0:4 offset1:5
	ds_read2st64_b32 v[82:83], v243 offset0:6 offset1:7
	ds_read2st64_b32 v[118:119], v243 offset0:8 offset1:9
	ds_read2st64_b32 v[120:121], v243 offset0:10 offset1:11
	ds_read2st64_b32 v[122:123], v243 offset0:12 offset1:13
	ds_read2st64_b32 v[124:125], v243 offset0:14 offset1:15
	ds_read2st64_b32 v[126:127], v243 offset0:16 offset1:17
	ds_read2st64_b32 v[128:129], v243 offset0:18 offset1:19
	s_waitcnt vmcnt(3)
	ds_read2st64_b32 v[130:131], v243 offset0:20 offset1:21
	ds_read2st64_b32 v[132:133], v243 offset0:22 offset1:23
	s_waitcnt vmcnt(2)
	ds_read2st64_b32 v[134:135], v243 offset0:24 offset1:25
	ds_read2st64_b32 v[136:137], v243 offset0:26 offset1:27
	s_waitcnt vmcnt(1)
	ds_read2st64_b32 v[138:139], v243 offset0:28 offset1:29
	ds_read2st64_b32 v[140:141], v243 offset0:30 offset1:31
	ds_read2st64_b32 v[114:115], v243 offset0:32 offset1:33
	ds_read2st64_b32 v[116:117], v243 offset0:34 offset1:35
	ds_read2st64_b32 v[110:111], v243 offset0:36 offset1:37
	ds_read2st64_b32 v[112:113], v243 offset0:38 offset1:39
	ds_read2st64_b32 v[106:107], v243 offset0:40 offset1:41
	ds_read2st64_b32 v[108:109], v243 offset0:42 offset1:43
	ds_read2st64_b32 v[102:103], v243 offset0:44 offset1:45
	ds_read2st64_b32 v[104:105], v243 offset0:46 offset1:47
	ds_read2st64_b32 v[98:99], v243 offset0:48 offset1:49
	ds_read2st64_b32 v[100:101], v243 offset0:50 offset1:51
	ds_read2st64_b32 v[94:95], v243 offset0:52 offset1:53
	ds_read2st64_b32 v[96:97], v243 offset0:54 offset1:55
	ds_read2st64_b32 v[68:69], v243 offset0:56 offset1:57
	ds_read2st64_b32 v[70:71], v243 offset0:58 offset1:59
	ds_read2st64_b32 v[80:81], v243 offset0:60 offset1:61
	ds_read2st64_b32 v[84:85], v243 offset0:62 offset1:63
	v_mov_b32_e32 v184, v10
	s_movk_i32 s4, 0xc00
	v_mov_b32_e32 v205, v1
	s_waitcnt lgkmcnt(3)
	v_mov_b32_e32 v73, v68
	v_mul_f32_e32 v0, v185, v68
	v_pk_fma_f32 v[66:67], v[184:185], v[72:73], v[0:1] op_sel_hi:[1,1,0] neg_lo:[0,0,1] neg_hi:[0,0,1]
	v_mov_b32_e32 v184, v11
	v_mov_b32_e32 v73, v69
	s_waitcnt lgkmcnt(2)
	v_pk_mul_f32 v[10:11], v[196:197], v[70:71]
	v_mul_f32_e32 v0, v185, v69
	v_pk_fma_f32 v[70:71], v[12:13], v[72:73], v[10:11] op_sel_hi:[1,0,1] neg_lo:[0,0,1] neg_hi:[0,0,1]
	s_waitcnt lgkmcnt(1)
	v_pk_mul_f32 v[10:11], v[196:197], v[80:81]
	v_mov_b32_e32 v80, v50
	v_pk_fma_f32 v[14:15], v[14:15], v[72:73], v[10:11] op_sel_hi:[1,0,1] neg_lo:[0,0,1] neg_hi:[0,0,1]
	s_waitcnt lgkmcnt(0)
	v_pk_mul_f32 v[10:11], v[196:197], v[84:85]
	v_mov_b32_e32 v84, v74
	v_mov_b32_e32 v85, v76
	v_mov_b32_e32 v76, v75
	v_mov_b32_e32 v81, v52
	v_pk_mul_f32 v[84:85], v[196:197], v[84:85]
	v_mov_b32_e32 v52, v51
	v_pk_mul_f32 v[50:51], v[196:197], v[76:77]
	v_pk_fma_f32 v[84:85], v[80:81], v[72:73], v[84:85] op_sel_hi:[1,0,1] neg_lo:[0,0,1] neg_hi:[0,0,1]
	v_pk_fma_f32 v[86:87], v[52:53], v[72:73], v[50:51] op_sel_hi:[1,0,1] neg_lo:[0,0,1] neg_hi:[0,0,1]
	s_waitcnt vmcnt(0)
	v_pk_mul_f32 v[142:143], v[84:85], v[84:85]
	v_pk_mul_f32 v[144:145], v[86:87], v[86:87]
	v_mov_b32_e32 v52, v78
	v_mov_b32_e32 v53, v82
	v_pk_fma_f32 v[68:69], v[184:185], v[72:73], v[0:1] op_sel_hi:[1,1,0] neg_lo:[0,0,1] neg_hi:[0,0,1]
	v_mov_b32_e32 v50, v54
	v_mov_b32_e32 v51, v56
	v_pk_mul_f32 v[52:53], v[196:197], v[52:53]
	v_mov_b32_e32 v82, v79
	v_add_f32_e32 v0, v142, v144
	v_pk_fma_f32 v[80:81], v[50:51], v[72:73], v[52:53] op_sel_hi:[1,0,1] neg_lo:[0,0,1] neg_hi:[0,0,1]
	v_mov_b32_e32 v56, v55
	v_pk_mul_f32 v[50:51], v[196:197], v[82:83]
	v_add_f32_e32 v0, v0, v143
	v_pk_mul_f32 v[146:147], v[80:81], v[80:81]
	v_pk_fma_f32 v[82:83], v[56:57], v[72:73], v[50:51] op_sel_hi:[1,0,1] neg_lo:[0,0,1] neg_hi:[0,0,1]
	v_add_f32_e32 v0, v0, v145
	v_pk_mul_f32 v[148:149], v[82:83], v[82:83]
	v_mov_b32_e32 v52, v118
	v_mov_b32_e32 v53, v120
	v_add_f32_e32 v0, v0, v146
	v_mov_b32_e32 v50, v58
	v_mov_b32_e32 v51, v60
	v_pk_mul_f32 v[52:53], v[196:197], v[52:53]
	v_mov_b32_e32 v120, v119
	v_add_f32_e32 v0, v0, v148
	v_pk_fma_f32 v[76:77], v[50:51], v[72:73], v[52:53] op_sel_hi:[1,0,1] neg_lo:[0,0,1] neg_hi:[0,0,1]
	v_mov_b32_e32 v60, v59
	v_pk_mul_f32 v[50:51], v[196:197], v[120:121]
	v_add_f32_e32 v0, v0, v147
	v_pk_mul_f32 v[150:151], v[76:77], v[76:77]
	v_pk_fma_f32 v[78:79], v[60:61], v[72:73], v[50:51] op_sel_hi:[1,0,1] neg_lo:[0,0,1] neg_hi:[0,0,1]
	v_add_f32_e32 v0, v0, v149
	v_pk_mul_f32 v[118:119], v[78:79], v[78:79]
	v_mov_b32_e32 v52, v122
	v_mov_b32_e32 v53, v124
	v_add_f32_e32 v0, v0, v150
	v_mov_b32_e32 v50, v62
	v_mov_b32_e32 v51, v64
	v_pk_mul_f32 v[52:53], v[196:197], v[52:53]
	v_mov_b32_e32 v124, v123
	v_add_f32_e32 v0, v0, v118
	v_pk_fma_f32 v[74:75], v[50:51], v[72:73], v[52:53] op_sel_hi:[1,0,1] neg_lo:[0,0,1] neg_hi:[0,0,1]
	v_mov_b32_e32 v64, v63
	v_pk_mul_f32 v[50:51], v[196:197], v[124:125]
	v_add_f32_e32 v0, v0, v151
	v_pk_fma_f32 v[16:17], v[16:17], v[72:73], v[10:11] op_sel_hi:[1,0,1] neg_lo:[0,0,1] neg_hi:[0,0,1]
	global_load_dwordx4 v[10:13], v[186:187], off
	global_load_dwordx4 v[142:145], v[186:187], off offset:32
	global_load_dwordx4 v[146:149], v[186:187], off offset:64
	global_load_dwordx4 v[150:153], v[186:187], off offset:96
	global_load_dwordx4 v[154:157], v[186:187], off offset:128
	global_load_dwordx4 v[158:161], v[186:187], off offset:160
	global_load_dwordx4 v[162:165], v[186:187], off offset:192
	global_load_dwordx4 v[166:169], v[186:187], off offset:224
	global_load_dwordx4 v[170:173], v[186:187], off offset:256
	global_load_dwordx4 v[174:177], v[186:187], off offset:288
	global_load_dwordx4 v[216:219], v[186:187], off offset:320
	v_pk_mul_f32 v[120:121], v[74:75], v[74:75]
	v_pk_fma_f32 v[62:63], v[64:65], v[72:73], v[50:51] op_sel_hi:[1,0,1] neg_lo:[0,0,1] neg_hi:[0,0,1]
	v_add_f32_e32 v0, v0, v119
	v_pk_mul_f32 v[64:65], v[62:63], v[62:63]
	v_mov_b32_e32 v52, v126
	v_mov_b32_e32 v53, v128
	v_add_f32_e32 v0, v0, v120
	v_mov_b32_e32 v50, v34
	v_mov_b32_e32 v51, v36
	v_pk_mul_f32 v[52:53], v[196:197], v[52:53]
	v_mov_b32_e32 v128, v127
	v_add_f32_e32 v0, v0, v64
	v_pk_fma_f32 v[58:59], v[50:51], v[72:73], v[52:53] op_sel_hi:[1,0,1] neg_lo:[0,0,1] neg_hi:[0,0,1]
	v_mov_b32_e32 v36, v35
	v_pk_mul_f32 v[34:35], v[196:197], v[128:129]
	v_add_f32_e32 v0, v0, v121
	v_pk_mul_f32 v[122:123], v[58:59], v[58:59]
	v_pk_fma_f32 v[60:61], v[36:37], v[72:73], v[34:35] op_sel_hi:[1,0,1] neg_lo:[0,0,1] neg_hi:[0,0,1]
	v_add_f32_e32 v0, v0, v65
	v_pk_mul_f32 v[124:125], v[60:61], v[60:61]
	v_mov_b32_e32 v36, v130
	v_mov_b32_e32 v37, v132
	v_add_f32_e32 v0, v0, v122
	v_mov_b32_e32 v34, v38
	v_mov_b32_e32 v35, v40
	v_pk_mul_f32 v[36:37], v[196:197], v[36:37]
	v_mov_b32_e32 v132, v131
	v_add_f32_e32 v0, v0, v124
	v_pk_fma_f32 v[54:55], v[34:35], v[72:73], v[36:37] op_sel_hi:[1,0,1] neg_lo:[0,0,1] neg_hi:[0,0,1]
	v_mov_b32_e32 v40, v39
	v_pk_mul_f32 v[34:35], v[196:197], v[132:133]
	v_add_f32_e32 v0, v0, v123
	v_pk_mul_f32 v[126:127], v[54:55], v[54:55]
	v_pk_fma_f32 v[56:57], v[40:41], v[72:73], v[34:35] op_sel_hi:[1,0,1] neg_lo:[0,0,1] neg_hi:[0,0,1]
	v_add_f32_e32 v0, v0, v125
	v_pk_mul_f32 v[128:129], v[56:57], v[56:57]
	v_mov_b32_e32 v36, v134
	v_mov_b32_e32 v37, v136
	v_add_f32_e32 v0, v0, v126
	v_mov_b32_e32 v34, v42
	v_mov_b32_e32 v35, v44
	v_pk_mul_f32 v[36:37], v[196:197], v[36:37]
	v_mov_b32_e32 v136, v135
	v_add_f32_e32 v0, v0, v128
	v_pk_fma_f32 v[50:51], v[34:35], v[72:73], v[36:37] op_sel_hi:[1,0,1] neg_lo:[0,0,1] neg_hi:[0,0,1]
	v_mov_b32_e32 v44, v43
	v_pk_mul_f32 v[34:35], v[196:197], v[136:137]
	v_add_f32_e32 v0, v0, v127
	v_pk_mul_f32 v[130:131], v[50:51], v[50:51]
	v_pk_fma_f32 v[52:53], v[44:45], v[72:73], v[34:35] op_sel_hi:[1,0,1] neg_lo:[0,0,1] neg_hi:[0,0,1]
	v_add_f32_e32 v0, v0, v129
	v_pk_mul_f32 v[132:133], v[52:53], v[52:53]
	v_mov_b32_e32 v36, v138
	v_mov_b32_e32 v37, v140
	v_add_f32_e32 v0, v0, v130
	v_mov_b32_e32 v34, v46
	v_mov_b32_e32 v35, v48
	v_pk_mul_f32 v[36:37], v[196:197], v[36:37]
	v_mov_b32_e32 v140, v139
	v_add_f32_e32 v0, v0, v132
	v_pk_fma_f32 v[44:45], v[34:35], v[72:73], v[36:37] op_sel_hi:[1,0,1] neg_lo:[0,0,1] neg_hi:[0,0,1]
	v_mov_b32_e32 v48, v47
	v_pk_mul_f32 v[34:35], v[196:197], v[140:141]
	v_add_f32_e32 v0, v0, v131
	v_pk_mul_f32 v[134:135], v[44:45], v[44:45]
	v_pk_fma_f32 v[46:47], v[48:49], v[72:73], v[34:35] op_sel_hi:[1,0,1] neg_lo:[0,0,1] neg_hi:[0,0,1]
	v_add_f32_e32 v0, v0, v133
	v_pk_mul_f32 v[48:49], v[46:47], v[46:47]
	v_mov_b32_e32 v36, v114
	v_mov_b32_e32 v37, v116
	v_add_f32_e32 v0, v0, v134
	v_mov_b32_e32 v34, v18
	v_mov_b32_e32 v35, v20
	v_pk_mul_f32 v[36:37], v[196:197], v[36:37]
	v_mov_b32_e32 v116, v115
	v_add_f32_e32 v0, v0, v48
	v_pk_fma_f32 v[40:41], v[34:35], v[72:73], v[36:37] op_sel_hi:[1,0,1] neg_lo:[0,0,1] neg_hi:[0,0,1]
	v_mov_b32_e32 v20, v19
	v_pk_mul_f32 v[18:19], v[196:197], v[116:117]
	v_add_f32_e32 v0, v0, v135
	v_pk_mul_f32 v[136:137], v[40:41], v[40:41]
	v_pk_fma_f32 v[42:43], v[20:21], v[72:73], v[18:19] op_sel_hi:[1,0,1] neg_lo:[0,0,1] neg_hi:[0,0,1]
	v_add_f32_e32 v0, v0, v49
	v_pk_mul_f32 v[114:115], v[42:43], v[42:43]
	v_mov_b32_e32 v20, v110
	v_mov_b32_e32 v21, v112
	v_add_f32_e32 v0, v0, v136
	v_mov_b32_e32 v18, v22
	v_mov_b32_e32 v19, v24
	v_pk_mul_f32 v[20:21], v[196:197], v[20:21]
	v_mov_b32_e32 v112, v111
	v_add_f32_e32 v0, v0, v114
	v_pk_fma_f32 v[36:37], v[18:19], v[72:73], v[20:21] op_sel_hi:[1,0,1] neg_lo:[0,0,1] neg_hi:[0,0,1]
	v_mov_b32_e32 v24, v23
	v_pk_mul_f32 v[18:19], v[196:197], v[112:113]
	v_add_f32_e32 v0, v0, v137
	v_pk_mul_f32 v[116:117], v[36:37], v[36:37]
	v_pk_fma_f32 v[38:39], v[24:25], v[72:73], v[18:19] op_sel_hi:[1,0,1] neg_lo:[0,0,1] neg_hi:[0,0,1]
	v_add_f32_e32 v0, v0, v115
	v_pk_mul_f32 v[110:111], v[38:39], v[38:39]
	v_mov_b32_e32 v20, v106
	v_mov_b32_e32 v21, v108
	v_add_f32_e32 v0, v0, v116
	v_mov_b32_e32 v18, v26
	v_mov_b32_e32 v19, v28
	v_pk_mul_f32 v[20:21], v[196:197], v[20:21]
	v_mov_b32_e32 v108, v107
	v_add_f32_e32 v0, v0, v110
	v_pk_fma_f32 v[34:35], v[18:19], v[72:73], v[20:21] op_sel_hi:[1,0,1] neg_lo:[0,0,1] neg_hi:[0,0,1]
	v_mov_b32_e32 v28, v27
	v_pk_mul_f32 v[18:19], v[196:197], v[108:109]
	v_add_f32_e32 v0, v0, v117
	v_pk_mul_f32 v[112:113], v[34:35], v[34:35]
	v_pk_fma_f32 v[26:27], v[28:29], v[72:73], v[18:19] op_sel_hi:[1,0,1] neg_lo:[0,0,1] neg_hi:[0,0,1]
	v_add_f32_e32 v0, v0, v111
	v_pk_mul_f32 v[28:29], v[26:27], v[26:27]
	v_mov_b32_e32 v20, v102
	v_mov_b32_e32 v21, v104
	v_add_f32_e32 v0, v0, v112
	v_mov_b32_e32 v18, v30
	v_mov_b32_e32 v19, v32
	v_pk_mul_f32 v[20:21], v[196:197], v[20:21]
	v_mov_b32_e32 v104, v103
	v_add_f32_e32 v0, v0, v28
	v_pk_fma_f32 v[22:23], v[18:19], v[72:73], v[20:21] op_sel_hi:[1,0,1] neg_lo:[0,0,1] neg_hi:[0,0,1]
	v_mov_b32_e32 v32, v31
	v_pk_mul_f32 v[18:19], v[196:197], v[104:105]
	v_add_f32_e32 v0, v0, v113
	v_pk_mul_f32 v[106:107], v[22:23], v[22:23]
	v_pk_fma_f32 v[24:25], v[32:33], v[72:73], v[18:19] op_sel_hi:[1,0,1] neg_lo:[0,0,1] neg_hi:[0,0,1]
	v_add_f32_e32 v0, v0, v29
	v_pk_mul_f32 v[30:31], v[24:25], v[24:25]
	v_mov_b32_e32 v20, v98
	v_mov_b32_e32 v21, v100
	v_add_f32_e32 v0, v0, v106
	v_mov_b32_e32 v18, v2
	v_mov_b32_e32 v19, v4
	v_pk_mul_f32 v[20:21], v[196:197], v[20:21]
	v_mov_b32_e32 v100, v99
	v_add_f32_e32 v0, v0, v30
	v_pk_fma_f32 v[18:19], v[18:19], v[72:73], v[20:21] op_sel_hi:[1,0,1] neg_lo:[0,0,1] neg_hi:[0,0,1]
	v_mov_b32_e32 v4, v3
	v_pk_mul_f32 v[2:3], v[196:197], v[100:101]
	v_add_f32_e32 v0, v0, v107
	v_pk_mul_f32 v[32:33], v[18:19], v[18:19]
	v_pk_fma_f32 v[20:21], v[4:5], v[72:73], v[2:3] op_sel_hi:[1,0,1] neg_lo:[0,0,1] neg_hi:[0,0,1]
	v_add_f32_e32 v0, v0, v31
	v_pk_mul_f32 v[98:99], v[20:21], v[20:21]
	v_mov_b32_e32 v4, v94
	v_mov_b32_e32 v5, v96
	v_add_f32_e32 v0, v0, v32
	v_mov_b32_e32 v2, v6
	v_mov_b32_e32 v3, v8
	v_pk_mul_f32 v[4:5], v[196:197], v[4:5]
	v_mov_b32_e32 v96, v95
	v_add_f32_e32 v0, v0, v98
	v_pk_fma_f32 v[2:3], v[2:3], v[72:73], v[4:5] op_sel_hi:[1,0,1] neg_lo:[0,0,1] neg_hi:[0,0,1]
	v_mov_b32_e32 v8, v7
	v_pk_mul_f32 v[4:5], v[196:197], v[96:97]
	v_add_f32_e32 v0, v0, v33
	v_pk_mul_f32 v[100:101], v[2:3], v[2:3]
	v_pk_fma_f32 v[4:5], v[8:9], v[72:73], v[4:5] op_sel_hi:[1,0,1] neg_lo:[0,0,1] neg_hi:[0,0,1]
	v_add_f32_e32 v0, v0, v99
	v_pk_mul_f32 v[6:7], v[4:5], v[4:5]
	v_add_f32_e32 v0, v0, v100
	v_add_f32_e32 v0, v0, v6
	v_add_f32_e32 v0, v0, v101
	v_add_f32_e32 v0, v0, v7
	v_fmac_f32_e32 v0, v66, v66
	v_pk_mul_f32 v[88:89], v[70:71], v[70:71]
	v_fmac_f32_e32 v0, v68, v68
	v_add_f32_e32 v0, v0, v88
	v_pk_mul_f32 v[90:91], v[14:15], v[14:15]
	v_add_f32_e32 v0, v0, v89
	v_add_f32_e32 v0, v0, v90
	v_pk_mul_f32 v[92:93], v[16:17], v[16:17]
	v_add_f32_e32 v0, v0, v91
	v_add_f32_e32 v0, v0, v92
	v_add_f32_e32 v0, v0, v93
	ds_bpermute_b32 v8, v183, v0
	v_mov_b64_e32 v[6:7], s[12:13]
	v_mad_u64_u32 v[6:7], s[6:7], v206, s4, v[6:7]
	v_mad_i32_i24 v7, v207, s4, v7
	s_waitcnt lgkmcnt(0)
	v_add_f32_e32 v0, v0, v8
	v_fmamk_f32 v0, v0, 0x3c000000, v226
	v_mul_f32_e32 v8, 0x4f800000, v0
	v_cmp_gt_f32_e32 vcc, s89, v0
	v_lshl_add_u64 v[6:7], v[6:7], 0, s[96:97]
	v_lshl_add_u64 v[6:7], v[6:7], 0, v[204:205]
	v_cndmask_b32_e32 v0, v0, v8, vcc
	v_sqrt_f32_e32 v8, v0
	s_mov_b32 s4, 0x4c00000
	v_mov_b32_e32 v69, v71
	v_mov_b32_e32 v67, v70
	v_add_u32_e32 v9, -1, v8
	v_fma_f32 v28, -v9, v8, v0
	v_cmp_ge_f32_e64 s[38:39], 0, v28
	v_add_u32_e32 v28, 1, v8
	s_nop 0
	v_cndmask_b32_e64 v9, v8, v9, s[38:39]
	v_fma_f32 v8, -v28, v8, v0
	v_cmp_lt_f32_e64 s[38:39], 0, v8
	s_nop 1
	v_cndmask_b32_e64 v8, v9, v28, s[38:39]
	v_mul_f32_e32 v9, 0x37800000, v8
	v_cndmask_b32_e32 v8, v8, v9, vcc
	v_cmp_class_f32_e32 vcc, v0, v227
	s_waitcnt vmcnt(0)
	v_mov_b32_e32 v9, v12
	v_mov_b32_e32 v12, v11
	v_cndmask_b32_e32 v0, v8, v0, vcc
	v_div_scale_f32 v28, s[6:7], v0, v0, 1.0
	v_rcp_f32_e32 v29, v28
	v_mov_b32_e32 v8, v10
	s_mov_b64 s[6:7], 0x4c00800
	v_readlane_b32 s38, v255, 18
	v_fma_f32 v10, -v28, v29, 1.0
	v_fmac_f32_e32 v29, v10, v29
	v_div_scale_f32 v10, vcc, 1.0, v0, 1.0
	v_mul_f32_e32 v11, v10, v29
	v_fma_f32 v30, -v28, v11, v10
	v_fmac_f32_e32 v11, v30, v29
	v_fma_f32 v10, -v28, v11, v10
	v_div_fmas_f32 v10, v10, v29, v11
	v_div_fixup_f32 v0, v10, v0, 1.0
	v_mul_f32_e32 v0, v245, v0
	v_pk_mul_f32 v[10:11], v[84:85], v[0:1] op_sel_hi:[1,0]
	v_pk_mul_f32 v[26:27], v[26:27], v[0:1] op_sel_hi:[1,0]
	v_pk_mul_f32 v[8:9], v[8:9], v[10:11]
	v_pk_mul_f32 v[10:11], v[86:87], v[0:1] op_sel_hi:[1,0]
	v_pk_mul_f32 v[4:5], v[4:5], v[0:1] op_sel_hi:[1,0]
	v_pk_mul_f32 v[10:11], v[12:13], v[10:11]
	v_and_b32_sdwa v13, v8, v228 dst_sel:DWORD dst_unused:UNUSED_PAD src0_sel:WORD_1 src1_sel:DWORD
	v_and_b32_sdwa v12, v9, v228 dst_sel:DWORD dst_unused:UNUSED_PAD src0_sel:WORD_1 src1_sel:DWORD
	v_add3_u32 v8, v8, v13, s55
	v_and_b32_sdwa v13, v10, v228 dst_sel:DWORD dst_unused:UNUSED_PAD src0_sel:WORD_1 src1_sel:DWORD
	v_add3_u32 v9, v9, v12, s55
	v_and_b32_sdwa v12, v11, v228 dst_sel:DWORD dst_unused:UNUSED_PAD src0_sel:WORD_1 src1_sel:DWORD
	v_add3_u32 v10, v10, v13, s55
	v_add3_u32 v11, v11, v12, s55
	v_and_b32_e32 v10, 0xffff0000, v10
	v_and_b32_e32 v11, 0xffff0000, v11
	v_or_b32_sdwa v8, v10, v8 dst_sel:DWORD dst_unused:UNUSED_PAD src0_sel:DWORD src1_sel:WORD_1
	v_add_co_u32_e32 v10, vcc, s4, v6
	v_or_b32_sdwa v9, v11, v9 dst_sel:DWORD dst_unused:UNUSED_PAD src0_sel:DWORD src1_sel:WORD_1
	s_nop 0
	v_addc_co_u32_e32 v11, vcc, 0, v7, vcc
	global_store_dwordx2 v[10:11], v[8:9], off offset:2048
	v_pk_mul_f32 v[12:13], v[80:81], v[0:1] op_sel_hi:[1,0]
	v_lshl_add_u64 v[6:7], v[6:7], 0, s[6:7]
	v_pk_mul_f32 v[2:3], v[2:3], v[0:1] op_sel_hi:[1,0]
	v_readlane_b32 s39, v255, 19
	v_mov_b32_e32 v8, v142
	v_mov_b32_e32 v9, v143
	v_mov_b32_e32 v10, v144
	v_mov_b32_e32 v11, v145
	global_load_dwordx4 v[142:145], v[186:187], off offset:352
	v_mov_b32_e32 v28, v8
	v_mov_b32_e32 v29, v10
	v_pk_mul_f32 v[12:13], v[28:29], v[12:13]
	v_pk_mul_f32 v[28:29], v[82:83], v[0:1] op_sel_hi:[1,0]
	v_mov_b32_e32 v10, v9
	v_pk_mul_f32 v[8:9], v[10:11], v[28:29]
	v_and_b32_sdwa v10, v13, v228 dst_sel:DWORD dst_unused:UNUSED_PAD src0_sel:WORD_1 src1_sel:DWORD
	v_and_b32_sdwa v11, v12, v228 dst_sel:DWORD dst_unused:UNUSED_PAD src0_sel:WORD_1 src1_sel:DWORD
	v_add3_u32 v11, v12, v11, s55
	v_add3_u32 v10, v13, v10, s55
	v_and_b32_sdwa v12, v9, v228 dst_sel:DWORD dst_unused:UNUSED_PAD src0_sel:WORD_1 src1_sel:DWORD
	v_and_b32_sdwa v13, v8, v228 dst_sel:DWORD dst_unused:UNUSED_PAD src0_sel:WORD_1 src1_sel:DWORD
	v_add3_u32 v9, v9, v12, s55
	v_add3_u32 v8, v8, v13, s55
	v_and_b32_e32 v9, 0xffff0000, v9
	v_and_b32_e32 v8, 0xffff0000, v8
	v_or_b32_sdwa v9, v9, v10 dst_sel:DWORD dst_unused:UNUSED_PAD src0_sel:DWORD src1_sel:WORD_1
	v_or_b32_sdwa v8, v8, v11 dst_sel:DWORD dst_unused:UNUSED_PAD src0_sel:DWORD src1_sel:WORD_1
	global_store_dwordx2 v[6:7], v[8:9], off offset:16
	v_pk_mul_f32 v[12:13], v[76:77], v[0:1] op_sel_hi:[1,0]
	v_mov_b32_e32 v8, v146
	v_mov_b32_e32 v9, v147
	v_mov_b32_e32 v10, v148
	v_mov_b32_e32 v11, v149
	global_load_dwordx4 v[146:149], v[186:187], off offset:384
	v_mov_b32_e32 v28, v8
	v_mov_b32_e32 v29, v10
	v_pk_mul_f32 v[12:13], v[28:29], v[12:13]
	v_pk_mul_f32 v[28:29], v[78:79], v[0:1] op_sel_hi:[1,0]
	v_mov_b32_e32 v10, v9
	v_pk_mul_f32 v[8:9], v[10:11], v[28:29]
	v_and_b32_sdwa v10, v13, v228 dst_sel:DWORD dst_unused:UNUSED_PAD src0_sel:WORD_1 src1_sel:DWORD
	v_and_b32_sdwa v11, v12, v228 dst_sel:DWORD dst_unused:UNUSED_PAD src0_sel:WORD_1 src1_sel:DWORD
	v_add3_u32 v11, v12, v11, s55
	v_add3_u32 v10, v13, v10, s55
	v_and_b32_sdwa v12, v9, v228 dst_sel:DWORD dst_unused:UNUSED_PAD src0_sel:WORD_1 src1_sel:DWORD
	v_and_b32_sdwa v13, v8, v228 dst_sel:DWORD dst_unused:UNUSED_PAD src0_sel:WORD_1 src1_sel:DWORD
	v_add3_u32 v9, v9, v12, s55
	v_add3_u32 v8, v8, v13, s55
	v_and_b32_e32 v9, 0xffff0000, v9
	v_and_b32_e32 v8, 0xffff0000, v8
	v_or_b32_sdwa v9, v9, v10 dst_sel:DWORD dst_unused:UNUSED_PAD src0_sel:DWORD src1_sel:WORD_1
	v_or_b32_sdwa v8, v8, v11 dst_sel:DWORD dst_unused:UNUSED_PAD src0_sel:DWORD src1_sel:WORD_1
	global_store_dwordx2 v[6:7], v[8:9], off offset:32
	v_pk_mul_f32 v[12:13], v[74:75], v[0:1] op_sel_hi:[1,0]
	v_mov_b32_e32 v8, v150
	v_mov_b32_e32 v9, v151
	v_mov_b32_e32 v10, v152
	v_mov_b32_e32 v11, v153
	global_load_dwordx4 v[150:153], v[186:187], off offset:416
	v_mov_b32_e32 v28, v8
	v_mov_b32_e32 v29, v10
	v_pk_mul_f32 v[12:13], v[28:29], v[12:13]
	v_pk_mul_f32 v[28:29], v[62:63], v[0:1] op_sel_hi:[1,0]
	v_mov_b32_e32 v10, v9
	v_pk_mul_f32 v[8:9], v[10:11], v[28:29]
	v_and_b32_sdwa v10, v13, v228 dst_sel:DWORD dst_unused:UNUSED_PAD src0_sel:WORD_1 src1_sel:DWORD
	v_and_b32_sdwa v11, v12, v228 dst_sel:DWORD dst_unused:UNUSED_PAD src0_sel:WORD_1 src1_sel:DWORD
	v_add3_u32 v11, v12, v11, s55
	v_add3_u32 v10, v13, v10, s55
	v_and_b32_sdwa v12, v9, v228 dst_sel:DWORD dst_unused:UNUSED_PAD src0_sel:WORD_1 src1_sel:DWORD
	v_and_b32_sdwa v13, v8, v228 dst_sel:DWORD dst_unused:UNUSED_PAD src0_sel:WORD_1 src1_sel:DWORD
	v_add3_u32 v9, v9, v12, s55
	v_add3_u32 v8, v8, v13, s55
	v_and_b32_e32 v9, 0xffff0000, v9
	v_and_b32_e32 v8, 0xffff0000, v8
	v_or_b32_sdwa v9, v9, v10 dst_sel:DWORD dst_unused:UNUSED_PAD src0_sel:DWORD src1_sel:WORD_1
	v_or_b32_sdwa v8, v8, v11 dst_sel:DWORD dst_unused:UNUSED_PAD src0_sel:DWORD src1_sel:WORD_1
	global_store_dwordx2 v[6:7], v[8:9], off offset:48
	v_pk_mul_f32 v[28:29], v[60:61], v[0:1] op_sel_hi:[1,0]
	v_pk_mul_f32 v[12:13], v[58:59], v[0:1] op_sel_hi:[1,0]
	v_mov_b32_e32 v8, v154
	v_mov_b32_e32 v9, v155
	v_mov_b32_e32 v10, v156
	v_mov_b32_e32 v11, v157
	global_load_dwordx4 v[154:157], v[186:187], off offset:448
	v_mov_b32_e32 v31, v10
	v_mov_b32_e32 v10, v9
	v_mov_b32_e32 v30, v8
	v_pk_mul_f32 v[10:11], v[10:11], v[28:29]
	v_pk_mul_f32 v[8:9], v[30:31], v[12:13]
	v_and_b32_sdwa v28, v11, v228 dst_sel:DWORD dst_unused:UNUSED_PAD src0_sel:WORD_1 src1_sel:DWORD
	v_and_b32_sdwa v29, v10, v228 dst_sel:DWORD dst_unused:UNUSED_PAD src0_sel:WORD_1 src1_sel:DWORD
	v_and_b32_sdwa v12, v9, v228 dst_sel:DWORD dst_unused:UNUSED_PAD src0_sel:WORD_1 src1_sel:DWORD
	v_and_b32_sdwa v13, v8, v228 dst_sel:DWORD dst_unused:UNUSED_PAD src0_sel:WORD_1 src1_sel:DWORD
	v_add3_u32 v11, v11, v28, s55
	v_add3_u32 v10, v10, v29, s55
	v_add3_u32 v8, v8, v13, s55
	v_add3_u32 v9, v9, v12, s55
	v_and_b32_e32 v11, 0xffff0000, v11
	v_and_b32_e32 v10, 0xffff0000, v10
	v_or_b32_sdwa v9, v11, v9 dst_sel:DWORD dst_unused:UNUSED_PAD src0_sel:DWORD src1_sel:WORD_1
	v_or_b32_sdwa v8, v10, v8 dst_sel:DWORD dst_unused:UNUSED_PAD src0_sel:DWORD src1_sel:WORD_1
	global_store_dwordx2 v[6:7], v[8:9], off offset:64
	v_pk_mul_f32 v[28:29], v[56:57], v[0:1] op_sel_hi:[1,0]
	v_pk_mul_f32 v[12:13], v[54:55], v[0:1] op_sel_hi:[1,0]
	v_mov_b32_e32 v8, v158
	v_mov_b32_e32 v9, v159
	v_mov_b32_e32 v10, v160
	v_mov_b32_e32 v11, v161
	global_load_dwordx4 v[158:161], v[186:187], off offset:480
	v_mov_b32_e32 v31, v10
	v_mov_b32_e32 v10, v9
	v_mov_b32_e32 v30, v8
	v_pk_mul_f32 v[10:11], v[28:29], v[10:11]
	v_pk_mul_f32 v[8:9], v[12:13], v[30:31]
	v_and_b32_sdwa v28, v11, v228 dst_sel:DWORD dst_unused:UNUSED_PAD src0_sel:WORD_1 src1_sel:DWORD
	v_and_b32_sdwa v29, v10, v228 dst_sel:DWORD dst_unused:UNUSED_PAD src0_sel:WORD_1 src1_sel:DWORD
	v_and_b32_sdwa v12, v9, v228 dst_sel:DWORD dst_unused:UNUSED_PAD src0_sel:WORD_1 src1_sel:DWORD
	v_and_b32_sdwa v13, v8, v228 dst_sel:DWORD dst_unused:UNUSED_PAD src0_sel:WORD_1 src1_sel:DWORD
	v_add3_u32 v11, v11, v28, s55
	v_add3_u32 v10, v10, v29, s55
	v_add3_u32 v8, v8, v13, s55
	v_add3_u32 v9, v9, v12, s55
	v_and_b32_e32 v11, 0xffff0000, v11
	v_and_b32_e32 v10, 0xffff0000, v10
	v_or_b32_sdwa v9, v11, v9 dst_sel:DWORD dst_unused:UNUSED_PAD src0_sel:DWORD src1_sel:WORD_1
	v_or_b32_sdwa v8, v10, v8 dst_sel:DWORD dst_unused:UNUSED_PAD src0_sel:DWORD src1_sel:WORD_1
	global_store_dwordx2 v[6:7], v[8:9], off offset:80
	v_pk_mul_f32 v[28:29], v[52:53], v[0:1] op_sel_hi:[1,0]
	v_pk_mul_f32 v[12:13], v[50:51], v[0:1] op_sel_hi:[1,0]
	v_mov_b32_e32 v8, v162
	v_mov_b32_e32 v9, v163
	v_mov_b32_e32 v10, v164
	v_mov_b32_e32 v11, v165
	v_mov_b32_e32 v31, v10
	v_mov_b32_e32 v10, v9
	v_mov_b32_e32 v30, v8
	v_pk_mul_f32 v[10:11], v[28:29], v[10:11]
	v_pk_mul_f32 v[8:9], v[12:13], v[30:31]
	v_and_b32_sdwa v28, v11, v228 dst_sel:DWORD dst_unused:UNUSED_PAD src0_sel:WORD_1 src1_sel:DWORD
	v_and_b32_sdwa v29, v10, v228 dst_sel:DWORD dst_unused:UNUSED_PAD src0_sel:WORD_1 src1_sel:DWORD
	v_and_b32_sdwa v12, v9, v228 dst_sel:DWORD dst_unused:UNUSED_PAD src0_sel:WORD_1 src1_sel:DWORD
	v_and_b32_sdwa v13, v8, v228 dst_sel:DWORD dst_unused:UNUSED_PAD src0_sel:WORD_1 src1_sel:DWORD
	v_add3_u32 v11, v11, v28, s55
	v_add3_u32 v10, v10, v29, s55
	v_add3_u32 v8, v8, v13, s55
	v_add3_u32 v9, v9, v12, s55
	v_and_b32_e32 v11, 0xffff0000, v11
	v_and_b32_e32 v10, 0xffff0000, v10
	v_or_b32_sdwa v9, v11, v9 dst_sel:DWORD dst_unused:UNUSED_PAD src0_sel:DWORD src1_sel:WORD_1
	v_or_b32_sdwa v8, v10, v8 dst_sel:DWORD dst_unused:UNUSED_PAD src0_sel:DWORD src1_sel:WORD_1
	global_store_dwordx2 v[6:7], v[8:9], off offset:96
	v_pk_mul_f32 v[28:29], v[46:47], v[0:1] op_sel_hi:[1,0]
	v_pk_mul_f32 v[12:13], v[44:45], v[0:1] op_sel_hi:[1,0]
	v_mov_b32_e32 v8, v166
	v_mov_b32_e32 v9, v167
	v_mov_b32_e32 v10, v168
	v_mov_b32_e32 v11, v169
	v_mov_b32_e32 v31, v10
	v_mov_b32_e32 v10, v9
	v_mov_b32_e32 v30, v8
	v_pk_mul_f32 v[10:11], v[28:29], v[10:11]
	v_pk_mul_f32 v[8:9], v[12:13], v[30:31]
	v_and_b32_sdwa v28, v11, v228 dst_sel:DWORD dst_unused:UNUSED_PAD src0_sel:WORD_1 src1_sel:DWORD
	v_and_b32_sdwa v29, v10, v228 dst_sel:DWORD dst_unused:UNUSED_PAD src0_sel:WORD_1 src1_sel:DWORD
	v_and_b32_sdwa v12, v9, v228 dst_sel:DWORD dst_unused:UNUSED_PAD src0_sel:WORD_1 src1_sel:DWORD
	v_and_b32_sdwa v13, v8, v228 dst_sel:DWORD dst_unused:UNUSED_PAD src0_sel:WORD_1 src1_sel:DWORD
	v_add3_u32 v11, v11, v28, s55
	v_add3_u32 v10, v10, v29, s55
	v_add3_u32 v8, v8, v13, s55
	v_add3_u32 v9, v9, v12, s55
	v_and_b32_e32 v11, 0xffff0000, v11
	v_and_b32_e32 v10, 0xffff0000, v10
	v_or_b32_sdwa v9, v11, v9 dst_sel:DWORD dst_unused:UNUSED_PAD src0_sel:DWORD src1_sel:WORD_1
	v_or_b32_sdwa v8, v10, v8 dst_sel:DWORD dst_unused:UNUSED_PAD src0_sel:DWORD src1_sel:WORD_1
	global_store_dwordx2 v[6:7], v[8:9], off offset:112
	v_pk_mul_f32 v[28:29], v[42:43], v[0:1] op_sel_hi:[1,0]
	v_pk_mul_f32 v[12:13], v[40:41], v[0:1] op_sel_hi:[1,0]
	v_mov_b32_e32 v8, v170
	v_mov_b32_e32 v9, v171
	v_mov_b32_e32 v10, v172
	v_mov_b32_e32 v11, v173
	v_mov_b32_e32 v31, v10
	v_mov_b32_e32 v10, v9
	v_mov_b32_e32 v30, v8
	v_pk_mul_f32 v[10:11], v[28:29], v[10:11]
	v_pk_mul_f32 v[8:9], v[12:13], v[30:31]
	v_and_b32_sdwa v28, v11, v228 dst_sel:DWORD dst_unused:UNUSED_PAD src0_sel:WORD_1 src1_sel:DWORD
	v_and_b32_sdwa v29, v10, v228 dst_sel:DWORD dst_unused:UNUSED_PAD src0_sel:WORD_1 src1_sel:DWORD
	v_and_b32_sdwa v12, v9, v228 dst_sel:DWORD dst_unused:UNUSED_PAD src0_sel:WORD_1 src1_sel:DWORD
	v_and_b32_sdwa v13, v8, v228 dst_sel:DWORD dst_unused:UNUSED_PAD src0_sel:WORD_1 src1_sel:DWORD
	v_add3_u32 v11, v11, v28, s55
	v_add3_u32 v10, v10, v29, s55
	v_add3_u32 v8, v8, v13, s55
	v_add3_u32 v9, v9, v12, s55
	v_and_b32_e32 v11, 0xffff0000, v11
	v_and_b32_e32 v10, 0xffff0000, v10
	v_or_b32_sdwa v9, v11, v9 dst_sel:DWORD dst_unused:UNUSED_PAD src0_sel:DWORD src1_sel:WORD_1
	v_or_b32_sdwa v8, v10, v8 dst_sel:DWORD dst_unused:UNUSED_PAD src0_sel:DWORD src1_sel:WORD_1
	global_store_dwordx2 v[6:7], v[8:9], off offset:128
	v_pk_mul_f32 v[28:29], v[38:39], v[0:1] op_sel_hi:[1,0]
	v_pk_mul_f32 v[12:13], v[36:37], v[0:1] op_sel_hi:[1,0]
	v_mov_b32_e32 v8, v174
	v_mov_b32_e32 v9, v175
	v_mov_b32_e32 v10, v176
	v_mov_b32_e32 v11, v177
	v_mov_b32_e32 v31, v10
	v_mov_b32_e32 v10, v9
	v_mov_b32_e32 v30, v8
	v_pk_mul_f32 v[10:11], v[28:29], v[10:11]
	v_pk_mul_f32 v[8:9], v[12:13], v[30:31]
	v_and_b32_sdwa v28, v11, v228 dst_sel:DWORD dst_unused:UNUSED_PAD src0_sel:WORD_1 src1_sel:DWORD
	v_and_b32_sdwa v29, v10, v228 dst_sel:DWORD dst_unused:UNUSED_PAD src0_sel:WORD_1 src1_sel:DWORD
	v_and_b32_sdwa v12, v9, v228 dst_sel:DWORD dst_unused:UNUSED_PAD src0_sel:WORD_1 src1_sel:DWORD
	v_and_b32_sdwa v13, v8, v228 dst_sel:DWORD dst_unused:UNUSED_PAD src0_sel:WORD_1 src1_sel:DWORD
	v_add3_u32 v11, v11, v28, s55
	v_add3_u32 v10, v10, v29, s55
	v_add3_u32 v8, v8, v13, s55
	v_add3_u32 v9, v9, v12, s55
	v_and_b32_e32 v11, 0xffff0000, v11
	v_and_b32_e32 v10, 0xffff0000, v10
	v_or_b32_sdwa v9, v11, v9 dst_sel:DWORD dst_unused:UNUSED_PAD src0_sel:DWORD src1_sel:WORD_1
	v_or_b32_sdwa v8, v10, v8 dst_sel:DWORD dst_unused:UNUSED_PAD src0_sel:DWORD src1_sel:WORD_1
	global_store_dwordx2 v[6:7], v[8:9], off offset:144
	v_pk_mul_f32 v[12:13], v[34:35], v[0:1] op_sel_hi:[1,0]
	v_mov_b32_e32 v8, v216
	v_mov_b32_e32 v9, v217
	v_mov_b32_e32 v10, v218
	v_mov_b32_e32 v11, v219
	v_mov_b32_e32 v29, v10
	v_mov_b32_e32 v10, v9
	v_mov_b32_e32 v28, v8
	v_pk_mul_f32 v[10:11], v[26:27], v[10:11]
	v_pk_mul_f32 v[8:9], v[12:13], v[28:29]
	v_and_b32_sdwa v26, v11, v228 dst_sel:DWORD dst_unused:UNUSED_PAD src0_sel:WORD_1 src1_sel:DWORD
	v_and_b32_sdwa v27, v10, v228 dst_sel:DWORD dst_unused:UNUSED_PAD src0_sel:WORD_1 src1_sel:DWORD
	v_and_b32_sdwa v12, v9, v228 dst_sel:DWORD dst_unused:UNUSED_PAD src0_sel:WORD_1 src1_sel:DWORD
	v_and_b32_sdwa v13, v8, v228 dst_sel:DWORD dst_unused:UNUSED_PAD src0_sel:WORD_1 src1_sel:DWORD
	v_add3_u32 v11, v11, v26, s55
	v_add3_u32 v10, v10, v27, s55
	v_add3_u32 v8, v8, v13, s55
	v_add3_u32 v9, v9, v12, s55
	v_and_b32_e32 v11, 0xffff0000, v11
	v_and_b32_e32 v10, 0xffff0000, v10
	v_or_b32_sdwa v9, v11, v9 dst_sel:DWORD dst_unused:UNUSED_PAD src0_sel:DWORD src1_sel:WORD_1
	v_or_b32_sdwa v8, v10, v8 dst_sel:DWORD dst_unused:UNUSED_PAD src0_sel:DWORD src1_sel:WORD_1
	global_store_dwordx2 v[6:7], v[8:9], off offset:160
	v_pk_mul_f32 v[12:13], v[22:23], v[0:1] op_sel_hi:[1,0]
	v_pk_mul_f32 v[22:23], v[24:25], v[0:1] op_sel_hi:[1,0]
	s_waitcnt vmcnt(10)
	v_mov_b32_e32 v8, v142
	v_mov_b32_e32 v9, v143
	v_mov_b32_e32 v10, v144
	v_mov_b32_e32 v11, v145
	v_mov_b32_e32 v25, v10
	v_mov_b32_e32 v10, v9
	v_mov_b32_e32 v24, v8
	v_pk_mul_f32 v[10:11], v[22:23], v[10:11]
	v_pk_mul_f32 v[8:9], v[12:13], v[24:25]
	v_and_b32_sdwa v22, v11, v228 dst_sel:DWORD dst_unused:UNUSED_PAD src0_sel:WORD_1 src1_sel:DWORD
	v_and_b32_sdwa v23, v10, v228 dst_sel:DWORD dst_unused:UNUSED_PAD src0_sel:WORD_1 src1_sel:DWORD
	v_and_b32_sdwa v12, v9, v228 dst_sel:DWORD dst_unused:UNUSED_PAD src0_sel:WORD_1 src1_sel:DWORD
	v_and_b32_sdwa v13, v8, v228 dst_sel:DWORD dst_unused:UNUSED_PAD src0_sel:WORD_1 src1_sel:DWORD
	v_add3_u32 v11, v11, v22, s55
	v_add3_u32 v10, v10, v23, s55
	v_add3_u32 v8, v8, v13, s55
	v_add3_u32 v9, v9, v12, s55
	v_and_b32_e32 v11, 0xffff0000, v11
	v_and_b32_e32 v10, 0xffff0000, v10
	v_or_b32_sdwa v9, v11, v9 dst_sel:DWORD dst_unused:UNUSED_PAD src0_sel:DWORD src1_sel:WORD_1
	v_or_b32_sdwa v8, v10, v8 dst_sel:DWORD dst_unused:UNUSED_PAD src0_sel:DWORD src1_sel:WORD_1
	global_store_dwordx2 v[6:7], v[8:9], off offset:176
	v_pk_mul_f32 v[12:13], v[18:19], v[0:1] op_sel_hi:[1,0]
	v_pk_mul_f32 v[18:19], v[20:21], v[0:1] op_sel_hi:[1,0]
	s_waitcnt vmcnt(10)
	v_mov_b32_e32 v8, v146
	v_mov_b32_e32 v9, v147
	v_mov_b32_e32 v10, v148
	v_mov_b32_e32 v11, v149
	v_mov_b32_e32 v21, v10
	v_mov_b32_e32 v10, v9
	v_mov_b32_e32 v20, v8
	v_pk_mul_f32 v[10:11], v[18:19], v[10:11]
	v_pk_mul_f32 v[8:9], v[12:13], v[20:21]
	v_and_b32_sdwa v18, v11, v228 dst_sel:DWORD dst_unused:UNUSED_PAD src0_sel:WORD_1 src1_sel:DWORD
	v_and_b32_sdwa v19, v10, v228 dst_sel:DWORD dst_unused:UNUSED_PAD src0_sel:WORD_1 src1_sel:DWORD
	v_and_b32_sdwa v12, v9, v228 dst_sel:DWORD dst_unused:UNUSED_PAD src0_sel:WORD_1 src1_sel:DWORD
	v_and_b32_sdwa v13, v8, v228 dst_sel:DWORD dst_unused:UNUSED_PAD src0_sel:WORD_1 src1_sel:DWORD
	v_add3_u32 v11, v11, v18, s55
	v_add3_u32 v10, v10, v19, s55
	v_add3_u32 v8, v8, v13, s55
	v_add3_u32 v9, v9, v12, s55
	v_and_b32_e32 v11, 0xffff0000, v11
	v_and_b32_e32 v10, 0xffff0000, v10
	v_or_b32_sdwa v9, v11, v9 dst_sel:DWORD dst_unused:UNUSED_PAD src0_sel:DWORD src1_sel:WORD_1
	v_or_b32_sdwa v8, v10, v8 dst_sel:DWORD dst_unused:UNUSED_PAD src0_sel:DWORD src1_sel:WORD_1
	global_store_dwordx2 v[6:7], v[8:9], off offset:192
	s_waitcnt vmcnt(10)
	v_mov_b32_e32 v8, v150
	v_mov_b32_e32 v9, v151
	v_mov_b32_e32 v10, v152
	v_mov_b32_e32 v11, v153
	v_mov_b32_e32 v13, v10
	v_mov_b32_e32 v10, v9
	v_mov_b32_e32 v12, v8
	v_pk_mul_f32 v[4:5], v[4:5], v[10:11]
	v_pk_mul_f32 v[2:3], v[2:3], v[12:13]
	v_and_b32_sdwa v10, v5, v228 dst_sel:DWORD dst_unused:UNUSED_PAD src0_sel:WORD_1 src1_sel:DWORD
	v_and_b32_sdwa v11, v4, v228 dst_sel:DWORD dst_unused:UNUSED_PAD src0_sel:WORD_1 src1_sel:DWORD
	v_and_b32_sdwa v8, v3, v228 dst_sel:DWORD dst_unused:UNUSED_PAD src0_sel:WORD_1 src1_sel:DWORD
	v_and_b32_sdwa v9, v2, v228 dst_sel:DWORD dst_unused:UNUSED_PAD src0_sel:WORD_1 src1_sel:DWORD
	v_add3_u32 v5, v5, v10, s55
	v_add3_u32 v4, v4, v11, s55
	v_add3_u32 v2, v2, v9, s55
	v_add3_u32 v3, v3, v8, s55
	v_and_b32_e32 v5, 0xffff0000, v5
	v_and_b32_e32 v4, 0xffff0000, v4
	v_or_b32_sdwa v3, v5, v3 dst_sel:DWORD dst_unused:UNUSED_PAD src0_sel:DWORD src1_sel:WORD_1
	v_or_b32_sdwa v2, v4, v2 dst_sel:DWORD dst_unused:UNUSED_PAD src0_sel:DWORD src1_sel:WORD_1
	global_store_dwordx2 v[6:7], v[2:3], off offset:208
	v_pk_mul_f32 v[10:11], v[68:69], v[0:1] op_sel_hi:[1,0]
	v_pk_mul_f32 v[8:9], v[66:67], v[0:1] op_sel_hi:[1,0]
	s_waitcnt vmcnt(10)
	v_mov_b32_e32 v2, v154
	v_mov_b32_e32 v3, v155
	v_mov_b32_e32 v4, v156
	v_mov_b32_e32 v5, v157
	v_mov_b32_e32 v13, v4
	v_mov_b32_e32 v4, v3
	v_mov_b32_e32 v12, v2
	v_pk_mul_f32 v[4:5], v[10:11], v[4:5]
	v_pk_mul_f32 v[2:3], v[8:9], v[12:13]
	v_and_b32_sdwa v10, v5, v228 dst_sel:DWORD dst_unused:UNUSED_PAD src0_sel:WORD_1 src1_sel:DWORD
	v_and_b32_sdwa v11, v4, v228 dst_sel:DWORD dst_unused:UNUSED_PAD src0_sel:WORD_1 src1_sel:DWORD
	v_and_b32_sdwa v8, v3, v228 dst_sel:DWORD dst_unused:UNUSED_PAD src0_sel:WORD_1 src1_sel:DWORD
	v_and_b32_sdwa v9, v2, v228 dst_sel:DWORD dst_unused:UNUSED_PAD src0_sel:WORD_1 src1_sel:DWORD
	v_add3_u32 v5, v5, v10, s55
	v_add3_u32 v4, v4, v11, s55
	v_add3_u32 v2, v2, v9, s55
	v_add3_u32 v3, v3, v8, s55
	v_and_b32_e32 v5, 0xffff0000, v5
	v_and_b32_e32 v4, 0xffff0000, v4
	v_or_b32_sdwa v3, v5, v3 dst_sel:DWORD dst_unused:UNUSED_PAD src0_sel:DWORD src1_sel:WORD_1
	v_or_b32_sdwa v2, v4, v2 dst_sel:DWORD dst_unused:UNUSED_PAD src0_sel:DWORD src1_sel:WORD_1
	global_store_dwordx2 v[6:7], v[2:3], off offset:224
	v_mov_b32_e32 v8, v14
	v_mov_b32_e32 v9, v16
	v_mov_b32_e32 v16, v15
	v_pk_mul_f32 v[8:9], v[8:9], v[0:1] op_sel_hi:[1,0]
	v_pk_mul_f32 v[10:11], v[16:17], v[0:1] op_sel_hi:[1,0]
	s_waitcnt vmcnt(10)
	v_mov_b32_e32 v2, v158
	v_mov_b32_e32 v3, v159
	v_mov_b32_e32 v4, v160
	v_mov_b32_e32 v5, v161
	v_mov_b32_e32 v12, v2
	v_mov_b32_e32 v13, v4
	v_mov_b32_e32 v4, v3
	v_pk_mul_f32 v[2:3], v[8:9], v[12:13]
	v_pk_mul_f32 v[4:5], v[10:11], v[4:5]
	v_and_b32_sdwa v0, v3, v228 dst_sel:DWORD dst_unused:UNUSED_PAD src0_sel:WORD_1 src1_sel:DWORD
	v_and_b32_sdwa v9, v5, v228 dst_sel:DWORD dst_unused:UNUSED_PAD src0_sel:WORD_1 src1_sel:DWORD
	v_and_b32_sdwa v10, v4, v228 dst_sel:DWORD dst_unused:UNUSED_PAD src0_sel:WORD_1 src1_sel:DWORD
	v_and_b32_sdwa v8, v2, v228 dst_sel:DWORD dst_unused:UNUSED_PAD src0_sel:WORD_1 src1_sel:DWORD
	v_add3_u32 v0, v3, v0, s55
	v_add3_u32 v3, v5, v9, s55
	v_add3_u32 v4, v4, v10, s55
	v_add3_u32 v2, v2, v8, s55
	v_and_b32_e32 v3, 0xffff0000, v3
	v_and_b32_e32 v4, 0xffff0000, v4
	v_or_b32_sdwa v3, v3, v0 dst_sel:DWORD dst_unused:UNUSED_PAD src0_sel:DWORD src1_sel:WORD_1
	v_or_b32_sdwa v2, v4, v2 dst_sel:DWORD dst_unused:UNUSED_PAD src0_sel:DWORD src1_sel:WORD_1
	global_store_dwordx2 v[6:7], v[2:3], off offset:240
	s_branch .LBB0_1000
